# speedup vs baseline: 1.0748x; 1.0322x over previous
_Z10agg_kernelPKjPKiPKDF16_S4_PKfS4_S0_S2_S2_S2_S2_Pf:
	s_and_b32 s3, s2, 1
	s_lshr_b32 s4, s2, 1
	s_load_dwordx16 s[8:23], s[0:1], 0x0
	s_load_dwordx8 s[24:31], s[0:1], 0x40
	s_mul_i32 s6, s4, 0xc4
	s_sub_u32 s5, 0xc350, s6
	s_min_u32 s5, s5, 0xc4
	v_lshrrev_b32_e32 v2, 2, v0
	v_and_b32_e32 v1, 3, v0
	v_lshrrev_b32_e32 v13, 1, v1
	v_lshl_add_u32 v13, s3, 1, v13
	v_lshlrev_b32_e32 v13, 2, v13
	v_lshlrev_b32_e32 v1, 4, v1
	s_lshl_b32 s52, s4, 2
	s_waitcnt lgkmcnt(0)
	s_add_u32 s52, s10, s52
	s_addc_u32 s53, s11, 0
	s_load_dwordx2 s[32:33], s[52:53], 0x0
	s_load_dwordx2 s[36:37], s[52:53], 0x404
	v_add_u32_e32 v40, s6, v2
	v_min_u32_e32 v40, 0xc34f, v40
	v_lshlrev_b32_e32 v40, 6, v40
	v_add3_u32 v40, v40, v13, 16
	global_load_dword v3, v40, s[16:17]
	global_load_dword v4, v40, s[16:17] offset:32
	v_lshlrev_b32_e32 v62, 2, v0
	v_mov_b32_e32 v63, 0
	ds_write_b32 v62, v63 offset:24448
	v_cmp_gt_u32_e32 vcc, 0x200, v0
	s_and_saveexec_b64 s[60:61], vcc
	ds_write_b32 v62, v63 offset:28544
	s_mov_b64 exec, s[60:61]
	s_waitcnt lgkmcnt(0)
	s_sub_u32 s38, s33, s32
	s_sub_u32 s39, s37, s36
	s_lshl_b32 s52, s32, 2
	s_add_u32 s42, s8, s52
	s_addc_u32 s43, s9, 0
	s_add_u32 s52, s36, 0xc3500
	s_lshl_b32 s52, s52, 2
	s_add_u32 s44, s8, s52
	s_addc_u32 s45, s9, 0
	s_max_i32 s52, s38, 1
	s_sub_u32 s52, s52, 1
	s_max_i32 s53, s39, 1
	s_sub_u32 s53, s53, 1
	s_movk_i32 s46, 0x80
	s_movk_i32 s55, 0x62
	s_movk_i32 s47, 0x61a8
	v_min_u32_e32 v41, s52, v0
	v_lshlrev_b32_e32 v41, 2, v41
	global_load_dword v8, v41, s[42:43] nt
	v_min_u32_e32 v41, s53, v0
	v_lshlrev_b32_e32 v41, 2, v41
	global_load_dword v24, v41, s[44:45] nt
	v_add_u32_e32 v40, 0x400, v0
	v_min_u32_e32 v41, s52, v40
	v_lshlrev_b32_e32 v41, 2, v41
	global_load_dword v9, v41, s[42:43] nt
	v_min_u32_e32 v41, s53, v40
	v_lshlrev_b32_e32 v41, 2, v41
	global_load_dword v25, v41, s[44:45] nt
	v_add_u32_e32 v40, 0x800, v0
	v_min_u32_e32 v41, s52, v40
	v_lshlrev_b32_e32 v41, 2, v41
	global_load_dword v10, v41, s[42:43] nt
	v_min_u32_e32 v41, s53, v40
	v_lshlrev_b32_e32 v41, 2, v41
	global_load_dword v26, v41, s[44:45] nt
	v_add_u32_e32 v40, 0xc00, v0
	v_min_u32_e32 v41, s52, v40
	v_lshlrev_b32_e32 v41, 2, v41
	global_load_dword v11, v41, s[42:43] nt
	v_min_u32_e32 v41, s53, v40
	v_lshlrev_b32_e32 v41, 2, v41
	global_load_dword v27, v41, s[44:45] nt
	v_mov_b32_e32 v61, 1
	v_mov_b32_e32 v43, 0xc4
	s_barrier
	s_waitcnt vmcnt(7)
	v_bfe_u32 v28, v8, 16, 7
	v_bfe_u32 v42, v8, 23, 1
	v_and_b32_e32 v44, 0xffff, v8
	v_mad_u32_u24 v28, v42, s55, v28
	v_cmp_le_u32_e32 vcc, s47, v44
	v_lshlrev_b32_e32 v28, 2, v28
	s_nop 0
	v_cndmask_b32_e32 v42, 0, v43, vcc
	v_lshl_add_u32 v28, v42, 2, v28
	v_cmp_gt_u32_e32 vcc, s38, v0
	s_and_saveexec_b64 s[60:61], vcc
	ds_add_rtn_u32 v16, v28, v61 offset:24448
	s_mov_b64 exec, s[60:61]
	s_waitcnt vmcnt(6)
	v_bfe_u32 v32, v24, 16, 7
	v_bfe_u32 v42, v24, 23, 1
	v_and_b32_e32 v44, 0xffff, v24
	v_mad_u32_u24 v32, v42, s55, v32
	v_cmp_le_u32_e32 vcc, s47, v44
	v_lshlrev_b32_e32 v32, 2, v32
	s_nop 0
	v_cndmask_b32_e32 v42, 0, v43, vcc
	v_lshl_add_u32 v32, v42, 2, v32
	v_cmp_gt_u32_e32 vcc, s39, v0
	s_and_saveexec_b64 s[60:61], vcc
	ds_add_rtn_u32 v20, v32, v61 offset:26496
	s_mov_b64 exec, s[60:61]
	s_waitcnt vmcnt(5)
	v_add_u32_e32 v40, 0x400, v0
	v_bfe_u32 v29, v9, 16, 7
	v_bfe_u32 v42, v9, 23, 1
	v_and_b32_e32 v44, 0xffff, v9
	v_mad_u32_u24 v29, v42, s55, v29
	v_cmp_le_u32_e32 vcc, s47, v44
	v_lshlrev_b32_e32 v29, 2, v29
	s_nop 0
	v_cndmask_b32_e32 v42, 0, v43, vcc
	v_lshl_add_u32 v29, v42, 2, v29
	v_cmp_gt_u32_e32 vcc, s38, v40
	s_and_saveexec_b64 s[60:61], vcc
	ds_add_rtn_u32 v17, v29, v61 offset:24448
	s_mov_b64 exec, s[60:61]
	s_waitcnt vmcnt(4)
	v_bfe_u32 v33, v25, 16, 7
	v_bfe_u32 v42, v25, 23, 1
	v_and_b32_e32 v44, 0xffff, v25
	v_mad_u32_u24 v33, v42, s55, v33
	v_cmp_le_u32_e32 vcc, s47, v44
	v_lshlrev_b32_e32 v33, 2, v33
	s_nop 0
	v_cndmask_b32_e32 v42, 0, v43, vcc
	v_lshl_add_u32 v33, v42, 2, v33
	v_cmp_gt_u32_e32 vcc, s39, v40
	s_and_saveexec_b64 s[60:61], vcc
	ds_add_rtn_u32 v21, v33, v61 offset:26496
	s_mov_b64 exec, s[60:61]
	s_waitcnt vmcnt(3)
	v_add_u32_e32 v40, 0x800, v0
	v_bfe_u32 v30, v10, 16, 7
	v_bfe_u32 v42, v10, 23, 1
	v_and_b32_e32 v44, 0xffff, v10
	v_mad_u32_u24 v30, v42, s55, v30
	v_cmp_le_u32_e32 vcc, s47, v44
	v_lshlrev_b32_e32 v30, 2, v30
	s_nop 0
	v_cndmask_b32_e32 v42, 0, v43, vcc
	v_lshl_add_u32 v30, v42, 2, v30
	v_cmp_gt_u32_e32 vcc, s38, v40
	s_and_saveexec_b64 s[60:61], vcc
	ds_add_rtn_u32 v18, v30, v61 offset:24448
	s_mov_b64 exec, s[60:61]
	s_waitcnt vmcnt(2)
	v_bfe_u32 v34, v26, 16, 7
	v_bfe_u32 v42, v26, 23, 1
	v_and_b32_e32 v44, 0xffff, v26
	v_mad_u32_u24 v34, v42, s55, v34
	v_cmp_le_u32_e32 vcc, s47, v44
	v_lshlrev_b32_e32 v34, 2, v34
	s_nop 0
	v_cndmask_b32_e32 v42, 0, v43, vcc
	v_lshl_add_u32 v34, v42, 2, v34
	v_cmp_gt_u32_e32 vcc, s39, v40
	s_and_saveexec_b64 s[60:61], vcc
	ds_add_rtn_u32 v22, v34, v61 offset:26496
	s_mov_b64 exec, s[60:61]
	s_waitcnt vmcnt(1)
	v_add_u32_e32 v40, 0xc00, v0
	v_bfe_u32 v31, v11, 16, 7
	v_bfe_u32 v42, v11, 23, 1
	v_and_b32_e32 v44, 0xffff, v11
	v_mad_u32_u24 v31, v42, s55, v31
	v_cmp_le_u32_e32 vcc, s47, v44
	v_lshlrev_b32_e32 v31, 2, v31
	s_nop 0
	v_cndmask_b32_e32 v42, 0, v43, vcc
	v_lshl_add_u32 v31, v42, 2, v31
	v_cmp_gt_u32_e32 vcc, s38, v40
	s_and_saveexec_b64 s[60:61], vcc
	ds_add_rtn_u32 v19, v31, v61 offset:24448
	s_mov_b64 exec, s[60:61]
	s_waitcnt vmcnt(0)
	v_bfe_u32 v35, v27, 16, 7
	v_bfe_u32 v42, v27, 23, 1
	v_and_b32_e32 v44, 0xffff, v27
	v_mad_u32_u24 v35, v42, s55, v35
	v_cmp_le_u32_e32 vcc, s47, v44
	v_lshlrev_b32_e32 v35, 2, v35
	s_nop 0
	v_cndmask_b32_e32 v42, 0, v43, vcc
	v_lshl_add_u32 v35, v42, 2, v35
	v_cmp_gt_u32_e32 vcc, s39, v40
	s_and_saveexec_b64 s[60:61], vcc
	ds_add_rtn_u32 v23, v35, v61 offset:26496
	s_mov_b64 exec, s[60:61]
	s_waitcnt lgkmcnt(0)
	s_barrier
	ds_read_b32 v40, v62 offset:24448
	v_and_b32_e32 v44, 63, v0
	v_lshrrev_b32_e32 v45, 6, v0
	v_lshlrev_b32_e32 v45, 2, v45
	v_and_b32_e32 v52, 0x1ff, v0
	v_lshrrev_b32_e32 v51, 9, v0
	v_cmp_le_u32_e32 vcc, 0xc4, v52
	v_mov_b32_e32 v47, 31
	s_nop 0
	v_cndmask_b32_e64 v53, 0, 1, vcc
	v_mul_u32_u24_e32 v54, 0xc4, v53
	v_sub_u32_e32 v54, v52, v54
	v_lshl_add_u32 v53, v51, 1, v53
	s_waitcnt lgkmcnt(0)
	v_min_u32_e32 v55, 31, v40
	v_sub_u32_e32 v55, v47, v55
	v_and_b32_e32 v47, 3, v0
	v_lshl_or_b32 v55, v55, 2, v47
	v_lshl_add_u32 v55, v53, 7, v55
	v_lshlrev_b32_e32 v55, 2, v55
	v_cmp_gt_u32_e32 vcc, 0x188, v52
	s_and_saveexec_b64 s[60:61], vcc
	ds_add_rtn_u32 v51, v55, v61 offset:28544
	s_mov_b64 exec, s[60:61]
	v_mov_b32_e32 v41, v40
	s_nop 1
	v_add_u32_dpp v41, v41, v41 row_shr:1 row_mask:0xf bank_mask:0xf
	s_nop 1
	v_add_u32_dpp v41, v41, v41 row_shr:2 row_mask:0xf bank_mask:0xf
	s_nop 1
	v_add_u32_dpp v41, v41, v41 row_shr:4 row_mask:0xf bank_mask:0xf
	s_nop 1
	v_add_u32_dpp v41, v41, v41 row_shr:8 row_mask:0xf bank_mask:0xf
	s_nop 1
	v_add_u32_dpp v41, v41, v41 row_bcast:15 row_mask:0xa bank_mask:0xf
	s_nop 1
	v_add_u32_dpp v41, v41, v41 row_bcast:31 row_mask:0xc bank_mask:0xf
	v_cmp_eq_u32_e32 vcc, 63, v44
	s_and_saveexec_b64 s[60:61], vcc
	ds_write_b32 v45, v41 offset:21056
	s_mov_b64 exec, s[60:61]
	s_waitcnt lgkmcnt(0)
	s_barrier
	v_cmp_gt_u32_e32 vcc, 0x200, v0
	s_and_saveexec_b64 s[60:61], vcc
	s_cbranch_execz .Lagg_bins_done
	ds_read_b32 v48, v62 offset:28544
	s_waitcnt lgkmcnt(0)
	v_mov_b32_e32 v49, v48
	s_nop 1
	v_add_u32_dpp v49, v49, v49 row_shr:1 row_mask:0xf bank_mask:0xf
	s_nop 1
	v_add_u32_dpp v49, v49, v49 row_shr:2 row_mask:0xf bank_mask:0xf
	s_nop 1
	v_add_u32_dpp v49, v49, v49 row_shr:4 row_mask:0xf bank_mask:0xf
	s_nop 1
	v_add_u32_dpp v49, v49, v49 row_shr:8 row_mask:0xf bank_mask:0xf
	s_nop 1
	v_add_u32_dpp v49, v49, v49 row_bcast:15 row_mask:0xa bank_mask:0xf
	s_nop 1
	v_add_u32_dpp v49, v49, v49 row_bcast:31 row_mask:0xc bank_mask:0xf
	s_nop 0
	v_sub_u32_e32 v50, v49, v48
	ds_write_b32 v62, v50 offset:32640
	v_cmp_eq_u32_e32 vcc, 63, v44
	s_and_b64 exec, exec, vcc
	ds_write_b32 v45, v49 offset:36736

.Lagg_w0_done:
	s_mov_b64 exec, s[60:61]
	s_waitcnt lgkmcnt(0)
	s_barrier
	ds_read_b32 v46, v45 offset:21120
	v_mov_b32_e32 v47, 0
	ds_read_b32 v48, v47 offset:21212
	ds_read_b32 v49, v47 offset:21244
	ds_read_b32 v50, v55 offset:32640
	v_lshlrev_b32_e32 v44, 3, v53
	ds_read_b32 v44, v44 offset:36736
	v_sub_u32_e32 v41, v41, v40
	v_mul_u32_u24_e32 v47, 0xc4, v53
	s_waitcnt lgkmcnt(0)
	v_add_u32_e32 v41, v41, v46
	ds_write_b32 v62, v41 offset:14336
	v_and_b32_e32 v46, 0x100, v55
	v_cmp_ne_u32_e32 vcc, 0, v46
	s_nop 1
	v_cndmask_b32_e32 v44, 0, v44, vcc
	v_add_u32_e32 v50, v50, v44
	v_add_u32_e32 v50, v50, v51
	v_add_lshl_u32 v50, v50, v47, 1
	v_cmp_gt_u32_e32 vcc, 0x188, v52
	s_and_saveexec_b64 s[60:61], vcc
	ds_write_b16 v50, v54 offset:18432
	s_mov_b64 exec, s[60:61]
	v_max_u32_e32 v48, v48, v49
	s_nop 0
	v_readfirstlane_b32 s52, v48
	s_max_u32 s52, s52, s38
	s_max_u32 s52, s52, s39
	s_cmpk_le_u32 s52, 0xe00
	s_cselect_b32 s7, 1, 0
	s_waitcnt lgkmcnt(0)
	s_barrier
	s_cmp_eq_u32 s7, 0
	s_cbranch_scc1 .Lagg_scatter_done
	ds_read_b32 v48, v28 offset:14336
	ds_read_b32 v49, v29 offset:14336
	ds_read_b32 v50, v30 offset:14336
	ds_read_b32 v51, v31 offset:14336
	s_waitcnt lgkmcnt(3)
	v_add_u32_e32 v48, v48, v16
	v_lshlrev_b32_e32 v48, 1, v48
	s_waitcnt lgkmcnt(2)
	v_add_u32_e32 v49, v49, v17
	v_lshlrev_b32_e32 v49, 1, v49
	s_waitcnt lgkmcnt(1)
	v_add_u32_e32 v50, v50, v18
	v_lshlrev_b32_e32 v50, 1, v50
	s_waitcnt lgkmcnt(0)
	v_add_u32_e32 v51, v51, v19
	v_lshlrev_b32_e32 v51, 1, v51
	v_cmp_gt_u32_e32 vcc, s38, v0
	s_and_saveexec_b64 s[60:61], vcc
	ds_write_b16 v48, v8 offset:0
	s_mov_b64 exec, s[60:61]
	v_add_u32_e32 v40, 0x400, v0
	v_cmp_gt_u32_e32 vcc, s38, v40
	s_and_saveexec_b64 s[60:61], vcc
	ds_write_b16 v49, v9 offset:0
	s_mov_b64 exec, s[60:61]
	v_add_u32_e32 v40, 0x800, v0
	v_cmp_gt_u32_e32 vcc, s38, v40
	s_and_saveexec_b64 s[60:61], vcc
	ds_write_b16 v50, v10 offset:0
	s_mov_b64 exec, s[60:61]
	v_add_u32_e32 v40, 0xc00, v0
	v_cmp_gt_u32_e32 vcc, s38, v40
	s_and_saveexec_b64 s[60:61], vcc
	ds_write_b16 v51, v11 offset:0
	s_mov_b64 exec, s[60:61]
	ds_read_b32 v48, v32 offset:16384
	ds_read_b32 v49, v33 offset:16384
	ds_read_b32 v50, v34 offset:16384
	ds_read_b32 v51, v35 offset:16384
	s_waitcnt lgkmcnt(3)
	v_add_u32_e32 v48, v48, v20
	v_lshlrev_b32_e32 v48, 1, v48
	s_waitcnt lgkmcnt(2)
	v_add_u32_e32 v49, v49, v21
	v_lshlrev_b32_e32 v49, 1, v49
	s_waitcnt lgkmcnt(1)
	v_add_u32_e32 v50, v50, v22
	v_lshlrev_b32_e32 v50, 1, v50
	s_waitcnt lgkmcnt(0)
	v_add_u32_e32 v51, v51, v23
	v_lshlrev_b32_e32 v51, 1, v51
	v_cmp_gt_u32_e32 vcc, s39, v0
	s_and_saveexec_b64 s[60:61], vcc
	ds_write_b16 v48, v24 offset:7168
	s_mov_b64 exec, s[60:61]
	v_add_u32_e32 v40, 0x400, v0
	v_cmp_gt_u32_e32 vcc, s39, v40
	s_and_saveexec_b64 s[60:61], vcc
	ds_write_b16 v49, v25 offset:7168
	s_mov_b64 exec, s[60:61]
	v_add_u32_e32 v40, 0x800, v0
	v_cmp_gt_u32_e32 vcc, s39, v40
	s_and_saveexec_b64 s[60:61], vcc
	ds_write_b16 v50, v26 offset:7168
	s_mov_b64 exec, s[60:61]
	v_add_u32_e32 v40, 0xc00, v0
	v_cmp_gt_u32_e32 vcc, s39, v40
	s_and_saveexec_b64 s[60:61], vcc
	ds_write_b16 v51, v27 offset:7168
	s_mov_b64 exec, s[60:61]
.Lagg_scatter_done:
	v_and_b32_e32 v40, 1, v0
	v_cmp_eq_u32_e32 vcc, 0, v40
	s_movk_i32 s52, 0xc4
	v_cmp_gt_u32_e64 s[60:61], s52, v2
	s_and_b64 vcc, vcc, s[60:61]
	s_and_saveexec_b64 s[60:61], vcc
	v_bfe_u32 v40, v0, 1, 1
	v_mul_u32_u24_e32 v40, 0x310, v40
	v_lshl_add_u32 v40, v2, 2, v40
	ds_write_b32 v40, v3 offset:21248
	ds_write_b32 v40, v4 offset:22816
	s_mov_b64 exec, s[60:61]
	s_waitcnt vmcnt(0) lgkmcnt(0)
	s_barrier
	v_lshrrev_b32_e32 v40, 6, v0
	s_nop 0
	v_readfirstlane_b32 s41, v40
	s_cmp_gt_u32 s41, 12
	s_cbranch_scc1 .Lagg_exit
	v_mov_b32_e32 v15, 1.0
	s_lshl_b32 s52, s3, 8
	s_add_u32 s68, s30, s52
	s_addc_u32 s69, s31, 0
	s_mul_i32 s52, s3, 0x61a800
	s_add_u32 s70, s14, s52
	s_addc_u32 s71, s15, 0
	s_mul_i32 s52, s3, 0x61a800
	s_add_u32 s48, s12, s52
	s_addc_u32 s49, s13, 0
	s_lshl_b32 s52, s3, 7
	s_add_u32 s52, s18, s52
	s_addc_u32 s53, s19, 0
	v_lshlrev_b32_e32 v40, 1, v1
	global_load_dwordx4 v[16:19], v40, s[52:53]
	global_load_dwordx4 v[20:23], v40, s[52:53] offset:16
	global_load_dword v56, v13, s[20:21] offset:0
	global_load_dword v57, v13, s[20:21] offset:16
	s_waitcnt vmcnt(0)
	v_not_b32_e32 v58, v56
	v_and_b32_e32 v59, 0x7fffffff, v56
	v_cmp_gt_i32_e32 vcc, 0, v56
	s_nop 1
	v_cndmask_b32_e32 v56, v58, v59, vcc
	v_not_b32_e32 v58, v57
	v_and_b32_e32 v59, 0x7fffffff, v57
	v_cmp_gt_i32_e32 vcc, 0, v57
	s_nop 1
	v_cndmask_b32_e32 v57, v58, v59, vcc
	v_mov_b32_e32 v46, v56
	v_add_f32_e32 v14, v56, v57
	v_mul_f32_e32 v58, 0x3c23d70a, v14
	v_max_f32_e32 v14, v14, v58
	s_cmp_eq_u32 s7, 0
	s_cbranch_scc1 .Lagg_slow_0
	s_lshl_b32 s40, s41, 4
	v_bfe_u32 v63, v0, 2, 4
	v_add_u32_e32 v63, s40, v63
	v_cmp_gt_u32_e32 vcc, 0xc4, v63
	s_and_saveexec_b64 s[58:59], vcc
	s_cbranch_execz .Lagg_phasedone_0_0
	v_lshlrev_b32_e32 v63, 1, v63
	ds_read_u16 v60, v63 offset:18432
	v_lshrrev_b32_e32 v63, 2, v1
	s_waitcnt lgkmcnt(0)
	v_lshlrev_b32_e32 v61, 2, v60
	ds_read_b32 v58, v61 offset:14336
	ds_read_b32 v59, v61 offset:14340
	v_bfe_u32 v57, v0, 1, 1
	v_mul_u32_u24_e32 v57, 0x310, v57
	v_lshl_add_u32 v57, v60, 2, v57
	ds_read_b32 v57, v57 offset:21248
	v_lshl_add_u32 v61, v60, 4, v63
	v_mov_b32_e32 v45, 0
	v_mov_b32_e32 v48, 0
	v_mov_b32_e32 v49, 0
	v_mov_b32_e32 v50, 0
	v_mov_b32_e32 v51, 0
	v_mov_b32_e32 v52, 0
	v_mov_b32_e32 v53, 0
	v_mov_b32_e32 v54, 0
	v_mov_b32_e32 v55, 0
	s_waitcnt lgkmcnt(0)
	v_lshlrev_b32_e32 v41, 1, v58
	v_lshlrev_b32_e32 v42, 1, v59
	v_cmp_lt_u32_e32 vcc, v41, v42
	s_and_saveexec_b64 s[64:65], vcc
	s_cbranch_execz .Lagg_listdone_0_0
	ds_read_u16 v40, v41
	v_add_u32_e32 v41, 2, v41
	s_waitcnt lgkmcnt(0)
	v_mad_u32_u16 v24, v40, s46, v1
	global_load_dwordx4 v[28:31], v24, s[48:49] offset:64
	global_load_dwordx4 v[24:27], v24, s[48:49]
	s_waitcnt lgkmcnt(0)
	v_add_f32_e32 v47, v46, v57
	v_mul_f32_e32 v56, 0x3c23d70a, v47
	v_max_f32_e32 v47, v47, v56
	v_sub_f32_e32 v43, v57, v47
	v_mul_f32_e32 v43, 0.5, v43
	v_mul_f32_e32 v44, 0xbf7d70a4, v47

.Lagg_listdone_0_0:
	s_mov_b64 exec, s[64:65]
	s_waitcnt vmcnt(0)
	ds_write_b32 v61, v48 offset:24448
	ds_write_b32 v61, v49 offset:27584
	ds_write_b32 v61, v50 offset:30720
	ds_write_b32 v61, v51 offset:33856
	ds_write_b32 v61, v52 offset:36992
	ds_write_b32 v61, v53 offset:40128
	ds_write_b32 v61, v54 offset:43264
	ds_write_b32 v61, v55 offset:46400
	ds_write_b32 v61, v45 offset:49536
.Lagg_phasedone_0_0:
	s_mov_b64 exec, s[58:59]
	s_sub_u32 s40, 12, s41
	s_lshl_b32 s40, s40, 4
	v_bfe_u32 v63, v0, 2, 4
	v_add_u32_e32 v63, s40, v63
	v_cmp_gt_u32_e32 vcc, 0xc4, v63
	s_and_saveexec_b64 s[58:59], vcc
	s_cbranch_execz .Lagg_phasedone_0_1
	v_lshlrev_b32_e32 v63, 1, v63
	ds_read_u16 v60, v63 offset:18824
	v_lshrrev_b32_e32 v63, 2, v1
	s_waitcnt lgkmcnt(0)
	v_lshlrev_b32_e32 v61, 2, v60
	ds_read_b32 v58, v61 offset:15120
	ds_read_b32 v59, v61 offset:15124
	v_bfe_u32 v57, v0, 1, 1
	v_mul_u32_u24_e32 v57, 0x310, v57
	v_lshl_add_u32 v57, v60, 2, v57
	ds_read_b32 v57, v57 offset:21248
	v_lshl_add_u32 v61, v60, 4, v63
	v_add_u32_e32 v61, 0x6e40, v61
	v_mov_b32_e32 v45, 0
	v_mov_b32_e32 v48, 0
	v_mov_b32_e32 v49, 0
	v_mov_b32_e32 v50, 0
	v_mov_b32_e32 v51, 0
	v_mov_b32_e32 v52, 0
	v_mov_b32_e32 v53, 0
	v_mov_b32_e32 v54, 0
	v_mov_b32_e32 v55, 0
	s_waitcnt lgkmcnt(0)
	v_lshlrev_b32_e32 v41, 1, v58
	v_lshlrev_b32_e32 v42, 1, v59
	v_cmp_lt_u32_e32 vcc, v41, v42
	s_and_saveexec_b64 s[64:65], vcc
	s_cbranch_execz .Lagg_listdone_0_1
	ds_read_u16 v40, v41
	v_add_u32_e32 v41, 2, v41
	s_waitcnt lgkmcnt(0)
	v_mad_u32_u16 v24, v40, s46, v1
	global_load_dwordx4 v[28:31], v24, s[48:49] offset:64
	global_load_dwordx4 v[24:27], v24, s[48:49]
	s_waitcnt lgkmcnt(0)
	v_add_f32_e32 v47, v46, v57
	v_mul_f32_e32 v56, 0x3c23d70a, v47
	v_max_f32_e32 v47, v47, v56
	v_sub_f32_e32 v43, v57, v47
	v_mul_f32_e32 v43, 0.5, v43
	v_mul_f32_e32 v44, 0xbf7d70a4, v47

.Lagg_join_0:
	s_waitcnt vmcnt(0) lgkmcnt(0)
	s_barrier
	v_cmp_gt_u32_e32 vcc, s5, v2
	s_and_saveexec_b64 s[58:59], vcc
	v_lshlrev_b32_e32 v61, 2, v0
	v_add_u32_e32 v60, 0x6e40, v61
	ds_read_b32 v48, v61 offset:24448
	ds_read_b32 v49, v61 offset:27584
	ds_read_b32 v50, v61 offset:30720
	ds_read_b32 v51, v61 offset:33856
	ds_read_b32 v52, v61 offset:36992
	ds_read_b32 v53, v61 offset:40128
	ds_read_b32 v54, v61 offset:43264
	ds_read_b32 v55, v61 offset:46400
	ds_read_b32 v45, v61 offset:49536
	s_waitcnt lgkmcnt(0)
	ds_read_b32 v24, v60 offset:24448
	ds_read_b32 v25, v60 offset:27584
	ds_read_b32 v26, v60 offset:30720
	ds_read_b32 v27, v60 offset:33856
	ds_read_b32 v28, v60 offset:36992
	ds_read_b32 v29, v60 offset:40128
	ds_read_b32 v30, v60 offset:43264
	ds_read_b32 v31, v60 offset:46400
	ds_read_b32 v32, v60 offset:49536
	v_mov_b32_e32 v62, 0x3c003c00
	s_waitcnt lgkmcnt(0)
	s_barrier
	v_pk_fma_f16 v48, v24, v62, v48
	v_pk_fma_f16 v49, v25, v62, v49
	v_pk_fma_f16 v50, v26, v62, v50
	v_pk_fma_f16 v51, v27, v62, v51
	v_pk_fma_f16 v52, v28, v62, v52
	v_pk_fma_f16 v53, v29, v62, v53
	v_pk_fma_f16 v54, v30, v62, v54
	v_pk_fma_f16 v55, v31, v62, v55
	v_add_f32_e32 v45, v45, v32
	s_cbranch_execz .Lagg_end_0
	v_add_f32_e32 v47, v46, v3
	v_mul_f32_e32 v58, 0x3c23d70a, v47
	v_max_f32_e32 v47, v47, v58
	v_sub_f32_e32 v58, v14, v47
	v_exp_f32_e32 v58, v58
	v_mul_f32_e32 v59, 0x33000000, v45
	v_rcp_f32_e32 v42, v45
	v_mul_f32_e32 v58, 0x24e69595, v58
	v_fma_f32 v60, -v45, v42, 1.0
	v_cmp_ge_f32_e64 s[62:63], v59, v58
	v_cmp_eq_f32_e32 vcc, 0, v45
	v_fmac_f32_e32 v42, v60, v42
	s_nop 1
	v_cndmask_b32_e64 v42, v42, 0, vcc
	s_or_b64 s[62:63], s[62:63], vcc
	s_mov_b64 s[66:67], exec
	s_andn2_b64 exec, exec, s[62:63]
	s_cbranch_execnz .Lagg_gmax_0

.Lagg_end_0:
	s_mov_b64 exec, s[58:59]
	s_mul_i32 s52, s3, 0x61a800
	s_add_u32 s52, s52, 0xc35000
	s_add_u32 s48, s12, s52
	s_addc_u32 s49, s13, 0
	s_lshl_b32 s52, s3, 7
	s_add_u32 s52, s52, 0x100
	s_add_u32 s52, s18, s52
	s_addc_u32 s53, s19, 0
	v_lshlrev_b32_e32 v40, 1, v1
	global_load_dwordx4 v[16:19], v40, s[52:53]
	global_load_dwordx4 v[20:23], v40, s[52:53] offset:16
	global_load_dword v56, v13, s[20:21] offset:32
	global_load_dword v57, v13, s[20:21] offset:48
	s_waitcnt vmcnt(0)
	v_not_b32_e32 v58, v56
	v_and_b32_e32 v59, 0x7fffffff, v56
	v_cmp_gt_i32_e32 vcc, 0, v56
	s_nop 1
	v_cndmask_b32_e32 v56, v58, v59, vcc
	v_not_b32_e32 v58, v57
	v_and_b32_e32 v59, 0x7fffffff, v57
	v_cmp_gt_i32_e32 vcc, 0, v57
	s_nop 1
	v_cndmask_b32_e32 v57, v58, v59, vcc
	v_mov_b32_e32 v46, v56
	v_add_f32_e32 v14, v56, v57
	v_mul_f32_e32 v58, 0x3c23d70a, v14
	v_max_f32_e32 v14, v14, v58
	s_cmp_eq_u32 s7, 0
	s_cbranch_scc1 .Lagg_slow_1
	s_sub_u32 s40, 12, s41
	s_lshl_b32 s40, s40, 4
	v_bfe_u32 v63, v0, 2, 4
	v_add_u32_e32 v63, s40, v63
	v_cmp_gt_u32_e32 vcc, 0xc4, v63
	s_and_saveexec_b64 s[58:59], vcc
	s_cbranch_execz .Lagg_phasedone_1_0
	v_lshlrev_b32_e32 v63, 1, v63
	ds_read_u16 v60, v63 offset:19216
	v_lshrrev_b32_e32 v63, 2, v1
	s_waitcnt lgkmcnt(0)
	v_lshlrev_b32_e32 v61, 2, v60
	ds_read_b32 v58, v61 offset:16384
	ds_read_b32 v59, v61 offset:16388
	v_bfe_u32 v57, v0, 1, 1
	v_mul_u32_u24_e32 v57, 0x310, v57
	v_lshl_add_u32 v57, v60, 2, v57
	ds_read_b32 v57, v57 offset:22816
	v_lshl_add_u32 v61, v60, 4, v63
	v_mov_b32_e32 v45, 0
	v_mov_b32_e32 v48, 0
	v_mov_b32_e32 v49, 0
	v_mov_b32_e32 v50, 0
	v_mov_b32_e32 v51, 0
	v_mov_b32_e32 v52, 0
	v_mov_b32_e32 v53, 0
	v_mov_b32_e32 v54, 0
	v_mov_b32_e32 v55, 0
	s_waitcnt lgkmcnt(0)
	v_lshlrev_b32_e32 v41, 1, v58
	v_lshlrev_b32_e32 v42, 1, v59
	v_add_u32_e32 v41, 0x1c00, v41
	v_add_u32_e32 v42, 0x1c00, v42
	v_cmp_lt_u32_e32 vcc, v41, v42
	s_and_saveexec_b64 s[64:65], vcc
	s_cbranch_execz .Lagg_listdone_1_0
	ds_read_u16 v40, v41
	v_add_u32_e32 v41, 2, v41
	s_waitcnt lgkmcnt(0)
	v_mad_u32_u16 v24, v40, s46, v1
	global_load_dwordx4 v[28:31], v24, s[48:49] offset:64
	global_load_dwordx4 v[24:27], v24, s[48:49]
	s_waitcnt lgkmcnt(0)
	v_add_f32_e32 v47, v46, v57
	v_mul_f32_e32 v56, 0x3c23d70a, v47
	v_max_f32_e32 v47, v47, v56
	v_sub_f32_e32 v43, v57, v47
	v_mul_f32_e32 v43, 0.5, v43
	v_mul_f32_e32 v44, 0xbf7d70a4, v47

.Lagg_phasedone_1_0:
	s_mov_b64 exec, s[58:59]
	s_lshl_b32 s40, s41, 4
	v_bfe_u32 v63, v0, 2, 4
	v_add_u32_e32 v63, s40, v63
	v_cmp_gt_u32_e32 vcc, 0xc4, v63
	s_and_saveexec_b64 s[58:59], vcc
	s_cbranch_execz .Lagg_phasedone_1_1
	v_lshlrev_b32_e32 v63, 1, v63
	ds_read_u16 v60, v63 offset:19608
	v_lshrrev_b32_e32 v63, 2, v1
	s_waitcnt lgkmcnt(0)
	v_lshlrev_b32_e32 v61, 2, v60
	ds_read_b32 v58, v61 offset:17168
	ds_read_b32 v59, v61 offset:17172
	v_bfe_u32 v57, v0, 1, 1
	v_mul_u32_u24_e32 v57, 0x310, v57
	v_lshl_add_u32 v57, v60, 2, v57
	ds_read_b32 v57, v57 offset:22816
	v_lshl_add_u32 v61, v60, 4, v63
	v_add_u32_e32 v61, 0x6e40, v61
	v_mov_b32_e32 v45, 0
	v_mov_b32_e32 v48, 0
	v_mov_b32_e32 v49, 0
	v_mov_b32_e32 v50, 0
	v_mov_b32_e32 v51, 0
	v_mov_b32_e32 v52, 0
	v_mov_b32_e32 v53, 0
	v_mov_b32_e32 v54, 0
	v_mov_b32_e32 v55, 0
	s_waitcnt lgkmcnt(0)
	v_lshlrev_b32_e32 v41, 1, v58
	v_lshlrev_b32_e32 v42, 1, v59
	v_add_u32_e32 v41, 0x1c00, v41
	v_add_u32_e32 v42, 0x1c00, v42
	v_cmp_lt_u32_e32 vcc, v41, v42
	s_and_saveexec_b64 s[64:65], vcc
	s_cbranch_execz .Lagg_listdone_1_1
	ds_read_u16 v40, v41
	v_add_u32_e32 v41, 2, v41
	s_waitcnt lgkmcnt(0)
	v_mad_u32_u16 v24, v40, s46, v1
	global_load_dwordx4 v[28:31], v24, s[48:49] offset:64
	global_load_dwordx4 v[24:27], v24, s[48:49]
	s_waitcnt lgkmcnt(0)
	v_add_f32_e32 v47, v46, v57
	v_mul_f32_e32 v56, 0x3c23d70a, v47
	v_max_f32_e32 v47, v47, v56
	v_sub_f32_e32 v43, v57, v47
	v_mul_f32_e32 v43, 0.5, v43
	v_mul_f32_e32 v44, 0xbf7d70a4, v47

.Lagg_join_1:
	s_waitcnt vmcnt(0) lgkmcnt(0)
	s_barrier
	v_cmp_gt_u32_e32 vcc, s5, v2
	s_and_saveexec_b64 s[58:59], vcc
	v_lshlrev_b32_e32 v61, 2, v0
	v_add_u32_e32 v60, 0x6e40, v61
	ds_read_b32 v48, v61 offset:24448
	ds_read_b32 v49, v61 offset:27584
	ds_read_b32 v50, v61 offset:30720
	ds_read_b32 v51, v61 offset:33856
	ds_read_b32 v52, v61 offset:36992
	ds_read_b32 v53, v61 offset:40128
	ds_read_b32 v54, v61 offset:43264
	ds_read_b32 v55, v61 offset:46400
	ds_read_b32 v45, v61 offset:49536
	s_waitcnt lgkmcnt(0)
	ds_read_b32 v24, v60 offset:24448
	ds_read_b32 v25, v60 offset:27584
	ds_read_b32 v26, v60 offset:30720
	ds_read_b32 v27, v60 offset:33856
	ds_read_b32 v28, v60 offset:36992
	ds_read_b32 v29, v60 offset:40128
	ds_read_b32 v30, v60 offset:43264
	ds_read_b32 v31, v60 offset:46400
	ds_read_b32 v32, v60 offset:49536
	v_mov_b32_e32 v62, 0x3c003c00
	s_waitcnt lgkmcnt(0)
	s_barrier
	v_pk_fma_f16 v48, v24, v62, v48
	v_pk_fma_f16 v49, v25, v62, v49
	v_pk_fma_f16 v50, v26, v62, v50
	v_pk_fma_f16 v51, v27, v62, v51
	v_pk_fma_f16 v52, v28, v62, v52
	v_pk_fma_f16 v53, v29, v62, v53
	v_pk_fma_f16 v54, v30, v62, v54
	v_pk_fma_f16 v55, v31, v62, v55
	v_add_f32_e32 v45, v45, v32
	s_cbranch_execz .Lagg_end_1
	v_add_f32_e32 v47, v46, v4
	v_mul_f32_e32 v58, 0x3c23d70a, v47
	v_max_f32_e32 v47, v47, v58
	v_add_u32_e32 v61, s6, v2
	v_mad_u32_u24 v40, v61, s46, v1
	global_load_dwordx4 v[24:27], v40, s[70:71] nt
	global_load_dwordx4 v[28:31], v40, s[70:71] offset:64 nt
	v_lshlrev_b32_e32 v41, 9, v61
	v_lshl_add_u32 v41, v1, 2, v41
	v_sub_f32_e32 v58, v14, v47
	v_exp_f32_e32 v58, v58
	v_mul_f32_e32 v59, 0x33000000, v45
	v_rcp_f32_e32 v42, v45
	v_mul_f32_e32 v58, 0x24e69595, v58
	v_fma_f32 v60, -v45, v42, 1.0
	v_cmp_ge_f32_e64 s[62:63], v59, v58
	v_cmp_eq_f32_e32 vcc, 0, v45
	v_fmac_f32_e32 v42, v60, v42
	s_nop 1
	v_cndmask_b32_e64 v42, v42, 0, vcc
	s_or_b64 s[62:63], s[62:63], vcc
	s_mov_b64 s[66:67], exec
	s_andn2_b64 exec, exec, s[62:63]
	s_cbranch_execnz .Lagg_gmax_1

.Lagg_slowdone_0:
	v_lshlrev_b32_e32 v61, 2, v0
	ds_write_b32 v61, v48 offset:24448
	ds_write_b32 v61, v49 offset:27584
	ds_write_b32 v61, v50 offset:30720
	ds_write_b32 v61, v51 offset:33856
	ds_write_b32 v61, v52 offset:36992
	ds_write_b32 v61, v53 offset:40128
	ds_write_b32 v61, v54 offset:43264
	ds_write_b32 v61, v55 offset:46400
	ds_write_b32 v61, v45 offset:49536
	v_mov_b32_e32 v40, 0
	v_add_u32_e32 v61, 0x6e40, v61
	ds_write_b32 v61, v40 offset:24448
	ds_write_b32 v61, v40 offset:27584
	ds_write_b32 v61, v40 offset:30720
	ds_write_b32 v61, v40 offset:33856
	ds_write_b32 v61, v40 offset:36992
	ds_write_b32 v61, v40 offset:40128
	ds_write_b32 v61, v40 offset:43264
	ds_write_b32 v61, v40 offset:46400
	ds_write_b32 v61, v40 offset:49536
	s_mov_b64 exec, s[58:59]
	s_branch .Lagg_join_0

	.amdhsa_kernel _Z10agg_kernelPKjPKiPKDF16_S4_PKfS4_S0_S2_S2_S2_S2_Pf
		.amdhsa_group_segment_fixed_size 80896
		.amdhsa_private_segment_fixed_size 0
		.amdhsa_kernarg_size 96
		.amdhsa_user_sgpr_count 2
		.amdhsa_user_sgpr_dispatch_ptr 0
		.amdhsa_user_sgpr_queue_ptr 0
		.amdhsa_user_sgpr_kernarg_segment_ptr 1
		.amdhsa_user_sgpr_dispatch_id 0
		.amdhsa_user_sgpr_kernarg_preload_length 0
		.amdhsa_user_sgpr_kernarg_preload_offset 0
		.amdhsa_user_sgpr_private_segment_size 0
		.amdhsa_uses_dynamic_stack 0
		.amdhsa_enable_private_segment 0
		.amdhsa_system_sgpr_workgroup_id_x 1
		.amdhsa_system_sgpr_workgroup_id_y 0
		.amdhsa_system_sgpr_workgroup_id_z 0
		.amdhsa_system_sgpr_workgroup_info 0
		.amdhsa_system_vgpr_workitem_id 0
		.amdhsa_next_free_vgpr 64
		.amdhsa_next_free_sgpr 72
		.amdhsa_accum_offset 64
		.amdhsa_reserve_vcc 1
		.amdhsa_float_round_mode_32 0
		.amdhsa_float_round_mode_16_64 0
		.amdhsa_float_denorm_mode_32 3
		.amdhsa_float_denorm_mode_16_64 3
		.amdhsa_dx10_clamp 1
		.amdhsa_ieee_mode 1
		.amdhsa_fp16_overflow 0
		.amdhsa_tg_split 0
		.amdhsa_exception_fp_ieee_invalid_op 0
		.amdhsa_exception_fp_denorm_src 0
		.amdhsa_exception_fp_ieee_div_zero 0
		.amdhsa_exception_fp_ieee_overflow 0
		.amdhsa_exception_fp_ieee_underflow 0
		.amdhsa_exception_fp_ieee_inexact 0
		.amdhsa_exception_int_div_zero 0
	.end_amdhsa_kernel

amdhsa.kernels:
  - .agpr_count:     0
    .args:
      - .actual_access:  read_only
        .address_space:  global
        .offset:         0
        .size:           8
        .value_kind:     global_buffer
      - .actual_access:  read_only
        .address_space:  global
        .offset:         8
        .size:           8
        .value_kind:     global_buffer
      - .actual_access:  read_only
        .address_space:  global
        .offset:         16
        .size:           8
        .value_kind:     global_buffer
      - .actual_access:  read_only
        .address_space:  global
        .offset:         24
        .size:           8
        .value_kind:     global_buffer
      - .actual_access:  read_only
        .address_space:  global
        .offset:         32
        .size:           8
        .value_kind:     global_buffer
      - .actual_access:  read_only
        .address_space:  global
        .offset:         40
        .size:           8
        .value_kind:     global_buffer
      - .actual_access:  read_only
        .address_space:  global
        .offset:         48
        .size:           8
        .value_kind:     global_buffer
      - .actual_access:  write_only
        .address_space:  global
        .offset:         56
        .size:           8
        .value_kind:     global_buffer
      - .actual_access:  write_only
        .address_space:  global
        .offset:         64
        .size:           8
        .value_kind:     global_buffer
      - .actual_access:  write_only
        .address_space:  global
        .offset:         72
        .size:           8
        .value_kind:     global_buffer
      - .actual_access:  write_only
        .address_space:  global
        .offset:         80
        .size:           8
        .value_kind:     global_buffer
      - .actual_access:  read_only
        .address_space:  global
        .offset:         88
        .size:           8
        .value_kind:     global_buffer
      - .actual_access:  read_only
        .address_space:  global
        .offset:         96
        .size:           8
        .value_kind:     global_buffer
      - .actual_access:  write_only
        .address_space:  global
        .offset:         104
        .size:           8
        .value_kind:     global_buffer
    .group_segment_fixed_size: 1024
    .kernarg_segment_align: 8
    .kernarg_segment_size: 112
    .language:       OpenCL C
    .language_version:
      - 2
      - 0
    .max_flat_workgroup_size: 1024
    .name:           _Z17prep_count_kernelPKfS0_S0_S0_S0_S0_S0_PDF16_PjPfS1_PKiS5_Pi
    .private_segment_fixed_size: 0
    .sgpr_count:     27
    .sgpr_spill_count: 0
    .symbol:         _Z17prep_count_kernelPKfS0_S0_S0_S0_S0_S0_PDF16_PjPfS1_PKiS5_Pi.kd
    .uniform_work_group_size: 1
    .uses_dynamic_stack: false
    .vgpr_count:     62
    .vgpr_spill_count: 0
    .wavefront_size: 64
  - .agpr_count:     0
    .args:
      - .actual_access:  read_only
        .address_space:  global
        .offset:         0
        .size:           8
        .value_kind:     global_buffer
      - .actual_access:  read_only
        .address_space:  global
        .offset:         8
        .size:           8
        .value_kind:     global_buffer
      - .actual_access:  read_only
        .address_space:  global
        .offset:         16
        .size:           8
        .value_kind:     global_buffer
      - .actual_access:  write_only
        .address_space:  global
        .offset:         24
        .size:           8
        .value_kind:     global_buffer
      - .actual_access:  write_only
        .address_space:  global
        .offset:         32
        .size:           8
        .value_kind:     global_buffer
      - .actual_access:  write_only
        .address_space:  global
        .offset:         40
        .size:           8
        .value_kind:     global_buffer
      - .address_space:  global
        .offset:         48
        .size:           8
        .value_kind:     global_buffer
      - .actual_access:  read_only
        .address_space:  global
        .offset:         56
        .size:           8
        .value_kind:     global_buffer
      - .actual_access:  read_only
        .address_space:  global
        .offset:         64
        .size:           8
        .value_kind:     global_buffer
      - .actual_access:  read_only
        .address_space:  global
        .offset:         72
        .size:           8
        .value_kind:     global_buffer
      - .actual_access:  read_only
        .address_space:  global
        .offset:         80
        .size:           8
        .value_kind:     global_buffer
      - .actual_access:  read_only
        .address_space:  global
        .offset:         88
        .size:           8
        .value_kind:     global_buffer
      - .actual_access:  write_only
        .address_space:  global
        .offset:         96
        .size:           8
        .value_kind:     global_buffer
      - .actual_access:  write_only
        .address_space:  global
        .offset:         104
        .size:           8
        .value_kind:     global_buffer
    .group_segment_fixed_size: 144320
    .kernarg_segment_align: 8
    .kernarg_segment_size: 112
    .language:       OpenCL C
    .language_version:
      - 2
      - 0
    .max_flat_workgroup_size: 512
    .name:           _Z19gemm_scatter_kernelPKfPKDF16_S0_PDF16_S3_PfPjPKiS7_S7_S7_S7_PiS5_
    .private_segment_fixed_size: 0
    .sgpr_count:     46
    .sgpr_spill_count: 0
    .symbol:         _Z19gemm_scatter_kernelPKfPKDF16_S0_PDF16_S3_PfPjPKiS7_S7_S7_S7_PiS5_.kd
    .uniform_work_group_size: 1
    .uses_dynamic_stack: false
    .vgpr_count:     230
    .vgpr_spill_count: 0
    .wavefront_size: 64
  - .agpr_count:     0
    .args:
      - .actual_access:  read_only
        .address_space:  global
        .offset:         0
        .size:           8
        .value_kind:     global_buffer
      - .actual_access:  read_only
        .address_space:  global
        .offset:         8
        .size:           8
        .value_kind:     global_buffer
      - .actual_access:  read_only
        .address_space:  global
        .offset:         16
        .size:           8
        .value_kind:     global_buffer
      - .actual_access:  read_only
        .address_space:  global
        .offset:         24
        .size:           8
        .value_kind:     global_buffer
      - .actual_access:  read_only
        .address_space:  global
        .offset:         32
        .size:           8
        .value_kind:     global_buffer
      - .actual_access:  read_only
        .address_space:  global
        .offset:         40
        .size:           8
        .value_kind:     global_buffer
      - .actual_access:  read_only
        .address_space:  global
        .offset:         48
        .size:           8
        .value_kind:     global_buffer
      - .actual_access:  read_only
        .address_space:  global
        .offset:         56
        .size:           8
        .value_kind:     global_buffer
      - .actual_access:  read_only
        .address_space:  global
        .offset:         64
        .size:           8
        .value_kind:     global_buffer
      - .actual_access:  read_only
        .address_space:  global
        .offset:         72
        .size:           8
        .value_kind:     global_buffer
      - .actual_access:  read_only
        .address_space:  global
        .offset:         80
        .size:           8
        .value_kind:     global_buffer
      - .actual_access:  write_only
        .address_space:  global
        .offset:         88
        .size:           8
        .value_kind:     global_buffer
    .group_segment_fixed_size: 80896
    .kernarg_segment_align: 8
    .kernarg_segment_size: 96
    .language:       OpenCL C
    .language_version:
      - 2
      - 0
    .max_flat_workgroup_size: 1024
    .name:           _Z10agg_kernelPKjPKiPKDF16_S4_PKfS4_S0_S2_S2_S2_S2_Pf
    .private_segment_fixed_size: 0
    .sgpr_count:     78
    .sgpr_spill_count: 0
    .symbol:         _Z10agg_kernelPKjPKiPKDF16_S4_PKfS4_S0_S2_S2_S2_S2_Pf.kd
    .uniform_work_group_size: 1
    .uses_dynamic_stack: false
    .vgpr_count:     64
    .vgpr_spill_count: 0
    .wavefront_size: 64
